# ret-scan v4: pipelined LDS reads, prefetch loads interleaved in step-1 MFMA stream, per-wave LDS transpose + stores inside step 2b
# baseline (speedup 1.0000x reference)
; #define LAS __attribute__((address_space(3)))
; __device__ __forceinline__ void phase_ret_scan(const bf16* PROJ, bf16* O, LAS unsigned char* lds, int tid, int vcu, int G) {
;     ...
;         const int b = unit >> 6, h = (unit >> 3) & 7, vsl = unit & 7;
;         const float lg = __log2f(1.0f - exp2f(-5.0f - (float)h));
;         const float g64 = exp2f(64.0f * lg);
;         f32x16 S[2][2];
; #pragma unroll
;         for (int a = 0; a < 2; ++a)
; #pragma unroll
;             for (int c = 0; c < 2; ++c) S[a][c] = zero16();
;         for (int i = tid; i < 33792 / 16; i += 512) *(LAS v4u*)(lds + ST + i * 16) = (v4u){0u, 0u, 0u, 0u};
;         v4u pq[4], pk[4], pv;
;         const __amdgpu_buffer_rsrc_t rsP = __builtin_amdgcn_make_buffer_rsrc((void*)(PROJ + (size_t)b * SEQ * RT_IN), (short)0, SEQ * RT_IN * 2, 0x00020000);
;         const __amdgpu_buffer_rsrc_t rsO = __builtin_amdgcn_make_buffer_rsrc((void*)(O + (size_t)b * SEQ * RT_V), (short)0, SEQ * RT_V * 2, 0x00020000);
;         const int vrow = tid >> 3, vch = tid & 7;
;         const unsigned voq = (unsigned)((tid >> 5) * RT_IN + (tid & 31) * 8) * 2u, vov = (unsigned)(vrow * RT_IN + vch * 8) * 2u;
;         const unsigned soq = (unsigned)(h * 256) * 2u, sok = (unsigned)(2048 + h * 256) * 2u, sov = (unsigned)(4096 + h * 512 + vsl * 64) * 2u;
;     ...
;         RS_PREFETCH(0);
;         float dec[16];
;         { const int a31 = lane & 31, a5 = lane >> 5, w4 = wave & 3, t_i = w4 >> 1, x_i = w4 & 1;
; #pragma unroll
;           for (int r = 0; r < 16; ++r) {
;               if (wave < 4) { const int t = 32 * x_i + a31, s = 32 * t_i + 8 * (r >> 2) + 4 * a5 + (r & 3); dec[r] = (s <= t) ? __builtin_amdgcn_exp2f((float)(t - s) * lg) : 0.f; }
;               else { const int t = 32 * t_i + (r & 3) + 8 * (r >> 2) + 4 * a5; dec[r] = __builtin_amdgcn_exp2f((float)(t + 1) * lg); } } }
;         unsigned opk[8];
; #pragma unroll
;         for (int i = 0; i < 8; ++i) opk[i] = 0u;
.Lrf_636:
	s_ashr_i32 s27, s26, 31
	s_lshr_b32 s80, s79, 3
	s_lshl_b64 s[4:5], s[26:27], 25
	v_readlane_b32 s92, v250, 4
	s_add_u32 s92, s7, s4
	s_addc_u32 s81, s11, s5
	s_and_b32 s4, s80, 7
	s_lshl_b32 s5, s4, 10
	s_lshl_b32 s27, s4, 9
	v_mul_f32_e32 v2, 0x42800000, v0
	s_mov_b32 s4, 0xc2fc0000
	s_lshl_b32 s26, s78, 1
	v_cmp_gt_f32_e32 vcc, s4, v2
	s_and_b32 s26, s26, 0x380
	s_or_b32 s5, s5, s26
	v_cndmask_b32_e32 v2, 0, v197, vcc
	v_fmac_f32_e32 v2, 0x42800000, v0
	s_or_b32 s26, s5, 0x182000
	v_exp_f32_e32 v2, v2
	v_mul_f32_e32 v0, v0, v169
	v_readlane_b32 s93, v250, 5
	s_and_b64 s[4:5], vcc, exec
	v_exp_f32_e32 v150, v0
	v_readlane_b32 s94, v250, 6
	v_readlane_b32 s95, v250, 7
	s_cselect_b32 s4, 0xffffffc0, 0
	s_and_b32 s93, s81, 0xffff
	v_or_b32_e32 v0, s9, v170
	v_writelane_b32 v250, s92, 4
	v_or_b32_e32 v0, s8, v0
	v_mov_b32_e32 v14, v1
	v_mov_b32_e32 v15, v1
	v_ldexp_f32 v148, v2, s4
	v_writelane_b32 v250, s93, 5
	v_lshlrev_b32_e32 v224, 1, v0
	v_mov_b32_e32 v0, v1
	v_mov_b32_e32 v2, v1
	v_mov_b32_e32 v3, v1
	v_mov_b32_e32 v4, v1
	v_mov_b32_e32 v5, v1
	v_mov_b32_e32 v6, v1
	v_mov_b32_e32 v7, v1
	v_mov_b32_e32 v8, v1
	v_mov_b32_e32 v9, v1
	v_mov_b32_e32 v10, v1
	v_mov_b32_e32 v11, v1
	v_mov_b32_e32 v12, v1
	v_mov_b32_e32 v13, v1
	s_waitcnt vmcnt(13)
	v_mov_b64_e32 v[30:31], v[14:15]
	v_mov_b64_e32 v[46:47], v[14:15]
	v_mov_b64_e32 v[62:63], v[14:15]
	v_mov_b64_e32 v[78:79], v[14:15]
	s_mov_b32 s80, 0
	v_writelane_b32 v250, s94, 6
	v_mov_b32_e32 v151, v150
	v_mov_b32_e32 v152, v148
	v_mov_b32_e32 v153, v148
	v_mov_b32_e32 v225, 0
	v_mov_b32_e32 v226, 0
	v_mov_b32_e32 v227, 0
	v_mov_b32_e32 v228, 0
	v_mov_b32_e32 v229, 0
	v_mov_b32_e32 v230, 0
	v_mov_b32_e32 v231, 0
	v_mov_b32_e32 v232, 0
	s_mov_b32 s81, 0
	v_mov_b64_e32 v[28:29], v[12:13]
	v_mov_b64_e32 v[26:27], v[10:11]
	v_mov_b64_e32 v[24:25], v[8:9]
	v_mov_b64_e32 v[22:23], v[6:7]
	v_mov_b64_e32 v[20:21], v[4:5]
	v_mov_b64_e32 v[18:19], v[2:3]
	v_mov_b64_e32 v[16:17], v[0:1]
	v_mov_b64_e32 v[44:45], v[12:13]
	v_mov_b64_e32 v[42:43], v[10:11]
	v_mov_b64_e32 v[40:41], v[8:9]
	v_mov_b64_e32 v[38:39], v[6:7]
	v_mov_b64_e32 v[36:37], v[4:5]
	v_mov_b64_e32 v[34:35], v[2:3]
	v_mov_b64_e32 v[32:33], v[0:1]
	v_mov_b64_e32 v[60:61], v[12:13]
	v_mov_b64_e32 v[58:59], v[10:11]
	v_mov_b64_e32 v[56:57], v[8:9]
	v_mov_b64_e32 v[54:55], v[6:7]
	v_mov_b64_e32 v[52:53], v[4:5]
	v_mov_b64_e32 v[50:51], v[2:3]
	v_mov_b64_e32 v[48:49], v[0:1]
	v_mov_b64_e32 v[76:77], v[12:13]
	v_mov_b64_e32 v[74:75], v[10:11]
	v_mov_b64_e32 v[72:73], v[8:9]
	v_mov_b64_e32 v[70:71], v[6:7]
	v_mov_b64_e32 v[68:69], v[4:5]
	v_mov_b64_e32 v[66:67], v[2:3]
	v_mov_b64_e32 v[64:65], v[0:1]
	v_writelane_b32 v250, s95, 7
	v_and_b32_e32 v169, 63, v165
	v_lshrrev_b32_e32 v191, 2, v169
	v_and_b32_e32 v190, 3, v169
	v_lshlrev_b32_e32 v201, 13, v191
	v_lshl_add_u32 v201, v190, 4, v201
	s_add_i32 s4, s8, s9
	s_add_i32 s4, s4, s13
	s_lshl_b32 s4, s4, 1
	s_lshl_b32 s5, s12, 13
	s_add_i32 s4, s4, s5
	v_add_u32_e32 v201, s4, v201
	v_mul_u32_u24_e32 v191, 0x50, v191
	v_lshl_add_u32 v191, v190, 4, v191
	s_lshr_b32 s4, s86, 6
	s_and_b32 s4, s4, 3
	s_mul_i32 s4, s4, 0xa00
	s_add_i32 s4, s4, 0x21000
	v_add_u32_e32 v191, s4, v191
	v_and_b32_e32 v190, 31, v169
	v_lshrrev_b32_e32 v169, 5, v169
	v_mul_u32_u24_e32 v169, 0x140, v169
	v_lshl_add_u32 v190, v190, 1, v169
	v_add_u32_e32 v190, s4, v190
	s_branch .Lrf_639

; #define LAS __attribute__((address_space(3)))
; __device__ __forceinline__ v4u scale_bf8(v4u q, float f) { v4u o; o.x = pk2(bflo(q.x) * f, bfhi(q.x) * f); o.y = pk2(bflo(q.y) * f, bfhi(q.y) * f); o.z = pk2(bflo(q.z) * f, bfhi(q.z) * f); o.w = pk2(bflo(q.w) * f, bfhi(q.w) * f); return o; }
; __device__ __forceinline__ void phase_ret_scan(const bf16* PROJ, bf16* O, LAS unsigned char* lds, int tid, int vcu, int G) {
;     ...
;         for (int ch = 0; ch < SEQ / 64; ++ch) {
; #pragma unroll
;             for (int i = 0; i < 4; ++i) { const int cid = tid + 512 * i, row = cid >> 5, chq = cid & 31;
;                 *(LAS v4u*)(lds + QN + row * QRS + chq * 16) = pq[i];
;                 *(LAS v4u*)(lds + KN + (chq >> 4) * 16384 + off_b(row, chq & 15)) = pk[i]; }
;             *(LAS v4u*)(lds + VV + off_b(vrow, vch)) = pv;
;             *(LAS v4u*)(lds + VV + off_b(vrow, 8 + vch)) = scale_bf8(pv, __builtin_amdgcn_exp2f((float)(63 - vrow) * lg));
;             __syncthreads();
.Lrf_639:
	s_cmp_eq_u32 s81, 0
	s_cbranch_scc1 .Lrf_w03
	s_and_b64 vcc, exec, s[0:1]
	s_cbranch_vccz .Lrf_w03
	s_waitcnt vmcnt(2)
	s_branch .Lrf_wgo

; #define LAS __attribute__((address_space(3)))
; __device__ __forceinline__ v4u scale_bf8(v4u q, float f) { v4u o; o.x = pk2(bflo(q.x) * f, bfhi(q.x) * f); o.y = pk2(bflo(q.y) * f, bfhi(q.y) * f); o.z = pk2(bflo(q.z) * f, bfhi(q.z) * f); o.w = pk2(bflo(q.w) * f, bfhi(q.w) * f); return o; }
; #define RS_MMA2(fa, fb) do { _Pragma("unroll") for (int j = 0; j < 2; ++j) acc = mfma32(fa[j], fb[j], acc); } while (0)
; #define RS_LD1B(fa, fb, g4) do { _Pragma("unroll") for (int j = 0; j < 2; ++j) { const int ks = 2 * (g4) + j; \
;                     fa[j] = *(const LAS s16x8*)(lds + QN + (32 * ti + a31) * QRS + (16 * ks + 8 * a5) * 2); \
;                     fb[j] = *(const LAS s16x8*)(lds + ST + (32 * vi + a31) * SRS + (16 * ks + 8 * a5) * 2); } } while (0)
; __device__ __forceinline__ void phase_ret_scan(const bf16* PROJ, bf16* O, LAS unsigned char* lds, int tid, int vcu, int G) {
;     ...
;         for (int ch = 0; ch < SEQ / 64; ++ch) {
; #pragma unroll
;             for (int i = 0; i < 4; ++i) { const int cid = tid + 512 * i, row = cid >> 5, chq = cid & 31;
;                 *(LAS v4u*)(lds + QN + row * QRS + chq * 16) = pq[i];
;                 *(LAS v4u*)(lds + KN + (chq >> 4) * 16384 + off_b(row, chq & 15)) = pk[i]; }
;             *(LAS v4u*)(lds + VV + off_b(vrow, vch)) = pv;
;             *(LAS v4u*)(lds + VV + off_b(vrow, 8 + vch)) = scale_bf8(pv, __builtin_amdgcn_exp2f((float)(63 - vrow) * lg));
;             __syncthreads();
;     ...
;             if (ch > 0) RS_STORE_O(ch - 1);
;             if (ch + 1 < SEQ / 64) RS_PREFETCH(ch + 1);
;     ...
;             } else {
;                 const int ti = t_i, vi = x_i;
;     ...
;                 RS_LD1B(fa0, fb0, 0); RS_LD1B(fa1, fb1, 1);
; #pragma unroll
;                 for (int g2 = 0; g2 < 3; ++g2) { RS_MMA2(fa0, fb0); RS_LD1B(fa0, fb0, 2 * g2 + 2); RS_MMA2(fa1, fb1); RS_LD1B(fa1, fb1, 2 * g2 + 3); }
;                 RS_MMA2(fa0, fb0); RS_MMA2(fa1, fb1);
;     ...
; #pragma unroll
;                 for (int r = 0; r < 16; ++r) acc[r] *= dec[r];
.Lrf_wgo:
	v_lshlrev_b32_e32 v2, 16, v128
	v_and_b32_e32 v3, 0xffff0000, v128
	v_lshlrev_b32_e32 v4, 16, v129
	v_and_b32_e32 v5, 0xffff0000, v129
	v_pk_mul_f32 v[2:3], v[150:151], v[2:3]
	v_pk_mul_f32 v[4:5], v[150:151], v[4:5]
	v_cvt_pk_bf16_f32 v2, v2, v3
	v_cvt_pk_bf16_f32 v3, v4, v5
	v_lshlrev_b32_e32 v4, 16, v130
	v_and_b32_e32 v5, 0xffff0000, v130
	v_lshlrev_b32_e32 v6, 16, v131
	v_and_b32_e32 v7, 0xffff0000, v131
	v_pk_mul_f32 v[4:5], v[150:151], v[4:5]
	v_pk_mul_f32 v[6:7], v[150:151], v[6:7]
	v_cvt_pk_bf16_f32 v4, v4, v5
	v_cvt_pk_bf16_f32 v5, v6, v7
	ds_write_b128 v214, v[96:99]
	ds_write_b128 v215, v[100:103] offset:33792
	ds_write_b128 v216, v[104:107]
	ds_write_b128 v217, v[108:111] offset:33792
	ds_write_b128 v218, v[112:115]
	ds_write_b128 v219, v[116:119] offset:33792
	ds_write_b128 v220, v[120:123]
	ds_write_b128 v221, v[124:127] offset:33792
	ds_write_b128 v222, v[128:131]
	ds_write_b128 v223, v[2:5]
	s_waitcnt lgkmcnt(0)
	s_barrier
.Lrf_643:
	v_mov_b32_e32 v2, v166
	s_and_b64 vcc, exec, s[74:75]
	v_and_b32_e32 v0, 31, v2
	v_ashrrev_i32_e32 v3, 5, v2
	s_mov_b64 s[4:5], -1
	s_cbranch_vccnz .Lrf_645
	s_add_i32 s100, s27, s80
	v_readlane_b32 s92, v250, 0
	v_readlane_b32 s93, v250, 1
	v_readlane_b32 s94, v250, 2
	v_readlane_b32 s95, v250, 3
	v_or_b32_e32 v4, s12, v0
	v_mul_u32_u24_e32 v4, 0x210, v4
	v_lshlrev_b32_e32 v8, 4, v3
	v_add3_u32 v12, 0, v4, v8
	v_or_b32_e32 v9, s13, v0
	v_mul_u32_u24_e32 v9, 0x210, v9
	s_add_i32 s4, 0, 0x16800
	v_add3_u32 v13, s4, v9, v8
	s_mov_b64 s[4:5], 0
	ds_read_b128 v[16:19], v12
	ds_read_b128 v[20:23], v13
	ds_read_b128 v[24:27], v12 offset:32
	ds_read_b128 v[28:31], v13 offset:32
	ds_read_b128 v[32:35], v12 offset:64
	ds_read_b128 v[36:39], v13 offset:64
	ds_read_b128 v[40:43], v12 offset:96
	ds_read_b128 v[44:47], v13 offset:96
	ds_read_b128 v[48:51], v12 offset:128
	ds_read_b128 v[52:55], v13 offset:128
	ds_read_b128 v[56:59], v12 offset:160
	ds_read_b128 v[60:63], v13 offset:160
	s_waitcnt lgkmcnt(10)
	v_mfma_f32_32x32x16_bf16 v[80:95], v[16:19], v[20:23], 0
	ds_read_b128 v[16:19], v12 offset:192
	ds_read_b128 v[20:23], v13 offset:192
	s_waitcnt lgkmcnt(10)
	v_mfma_f32_32x32x16_bf16 v[80:95], v[24:27], v[28:31], v[80:95]
	s_add_i32 s101, s100, 0x180000
	buffer_load_dwordx4 v[96:99], v167, s[92:95], s101 offen
	ds_read_b128 v[24:27], v12 offset:224
	ds_read_b128 v[28:31], v13 offset:224
	s_waitcnt lgkmcnt(10)
	v_mfma_f32_32x32x16_bf16 v[80:95], v[32:35], v[36:39], v[80:95]
	s_add_i32 s101, s100, 0x181000
	buffer_load_dwordx4 v[100:103], v167, s[92:95], s101 offen
	ds_read_b128 v[32:35], v12 offset:256
	ds_read_b128 v[36:39], v13 offset:256
	s_waitcnt lgkmcnt(10)
	v_mfma_f32_32x32x16_bf16 v[80:95], v[40:43], v[44:47], v[80:95]
	s_add_i32 s101, s100, 0x1e0000
	buffer_load_dwordx4 v[104:107], v167, s[92:95], s101 offen
	ds_read_b128 v[40:43], v12 offset:288
	ds_read_b128 v[44:47], v13 offset:288
	s_waitcnt lgkmcnt(10)
	v_mfma_f32_32x32x16_bf16 v[80:95], v[48:51], v[52:55], v[80:95]
	s_add_i32 s101, s100, 0x1e1000
	buffer_load_dwordx4 v[108:111], v167, s[92:95], s101 offen
	ds_read_b128 v[48:51], v12 offset:320
	ds_read_b128 v[52:55], v13 offset:320
	s_waitcnt lgkmcnt(10)
	v_mfma_f32_32x32x16_bf16 v[80:95], v[56:59], v[60:63], v[80:95]
	s_add_i32 s101, s100, 0x240000
	buffer_load_dwordx4 v[112:115], v167, s[92:95], s101 offen
	ds_read_b128 v[56:59], v12 offset:352
	ds_read_b128 v[60:63], v13 offset:352
	s_waitcnt lgkmcnt(10)
	v_mfma_f32_32x32x16_bf16 v[80:95], v[16:19], v[20:23], v[80:95]
	s_add_i32 s101, s100, 0x241000
	buffer_load_dwordx4 v[116:119], v167, s[92:95], s101 offen
	ds_read_b128 v[16:19], v12 offset:384
	ds_read_b128 v[20:23], v13 offset:384
	s_waitcnt lgkmcnt(10)
	v_mfma_f32_32x32x16_bf16 v[80:95], v[24:27], v[28:31], v[80:95]
	s_add_i32 s101, s100, 0x2a0000
	buffer_load_dwordx4 v[120:123], v167, s[92:95], s101 offen
	ds_read_b128 v[24:27], v12 offset:416
	ds_read_b128 v[28:31], v13 offset:416
	s_waitcnt lgkmcnt(10)
	v_mfma_f32_32x32x16_bf16 v[80:95], v[32:35], v[36:39], v[80:95]
	s_add_i32 s101, s100, 0x2a1000
	buffer_load_dwordx4 v[124:127], v167, s[92:95], s101 offen
	ds_read_b128 v[32:35], v12 offset:448
	ds_read_b128 v[36:39], v13 offset:448
	s_waitcnt lgkmcnt(10)
	v_mfma_f32_32x32x16_bf16 v[80:95], v[40:43], v[44:47], v[80:95]
	s_add_i32 s101, s26, s80
	buffer_load_dwordx4 v[128:131], v168, s[92:95], s101 offen
	ds_read_b128 v[40:43], v12 offset:480
	ds_read_b128 v[44:47], v13 offset:480
	s_waitcnt lgkmcnt(10)
	v_mfma_f32_32x32x16_bf16 v[80:95], v[48:51], v[52:55], v[80:95]
	s_waitcnt lgkmcnt(8)
	v_mfma_f32_32x32x16_bf16 v[80:95], v[56:59], v[60:63], v[80:95]
	s_waitcnt lgkmcnt(6)
	v_mfma_f32_32x32x16_bf16 v[80:95], v[16:19], v[20:23], v[80:95]
	s_waitcnt lgkmcnt(4)
	v_mfma_f32_32x32x16_bf16 v[80:95], v[24:27], v[28:31], v[80:95]
	s_waitcnt lgkmcnt(2)
	v_mfma_f32_32x32x16_bf16 v[80:95], v[32:35], v[36:39], v[80:95]
	s_waitcnt lgkmcnt(0)
	v_mfma_f32_32x32x16_bf16 v[80:95], v[40:43], v[44:47], v[80:95]
	s_nop 11
	v_pk_mul_f32 v[94:95], v[146:147], v[94:95]
	v_pk_mul_f32 v[92:93], v[144:145], v[92:93]
	v_pk_mul_f32 v[90:91], v[142:143], v[90:91]
	v_pk_mul_f32 v[88:89], v[140:141], v[88:89]
	v_pk_mul_f32 v[86:87], v[138:139], v[86:87]
	v_pk_mul_f32 v[84:85], v[136:137], v[84:85]
	v_pk_mul_f32 v[82:83], v[134:135], v[82:83]
	v_pk_mul_f32 v[80:81], v[132:133], v[80:81]
; #define LAS __attribute__((address_space(3)))
; __device__ __forceinline__ unsigned pk2(float lo, float hi) { const pk_f2 v = {lo, hi}; return __builtin_bit_cast(unsigned, __builtin_convertvector(v, pk_b2)); }
; #define RS_LD1A(fa, fb, g4) do { _Pragma("unroll") for (int j = 0; j < 2; ++j) { const int ks = 2 * (g4) + j; \
;                     fa[j] = *(const LAS s16x8*)(lds + KN + (ks >> 3) * 16384 + off_b(32 * si + a31, 2 * (ks & 7) + a5)); \
;                     fb[j] = *(const LAS s16x8*)(lds + QN + (32 * ti + a31) * QRS + (16 * ks + 8 * a5) * 2); } } while (0)
; #define RS_MMA2(fa, fb) do { _Pragma("unroll") for (int j = 0; j < 2; ++j) acc = mfma32(fa[j], fb[j], acc); } while (0)
; __device__ __forceinline__ void phase_ret_scan(const bf16* PROJ, bf16* O, LAS unsigned char* lds, int tid, int vcu, int G) {
;     ...
;             if (ch + 1 < SEQ / 64) RS_PREFETCH(ch + 1);
;             f32x16 acc = zero16();
;             int lnA = lane; asm volatile("" : "+v"(lnA));
;             const int a31 = lnA & 31, a5 = lnA >> 5;
;             const int w4 = wave & 3, t_i = w4 >> 1, x_i = w4 & 1;
;             s16x8 fa0[4], fb0[4], fa1[4], fb1[4];
;             if (wave < 4) {
;                 const int si = t_i, ti = x_i;
;     ...
;                 RS_LD1A(fa0, fb0, 0); RS_LD1A(fa1, fb1, 1);
; #pragma unroll
;                 for (int g2 = 0; g2 < 3; ++g2) { RS_MMA2(fa0, fb0); RS_LD1A(fa0, fb0, 2 * g2 + 2); RS_MMA2(fa1, fb1); RS_LD1A(fa1, fb1, 2 * g2 + 3); }
;                 RS_MMA2(fa0, fb0); RS_MMA2(fa1, fb1);
;     ...
;                 const int t = 32 * ti + a31;
; #pragma unroll
;                 for (int g = 0; g < 4; ++g) { float pvv[4];
; #pragma unroll
;                     for (int e = 0; e < 4; ++e) pvv[e] = acc[4 * g + e] * dec[4 * g + e];
;                     v2u w; w.x = pk2(pvv[0], pvv[1]); w.y = pk2(pvv[2], pvv[3]);
;                     *(LAS v2u*)(lds + PI + t * PRS + (32 * si + 8 * g + 4 * a5) * 2) = w; }
.Lrf_645:
	s_andn2_b64 vcc, exec, s[4:5]
	s_cbranch_vccnz .Lrf_647
	s_add_i32 s100, s27, s80
	v_readlane_b32 s92, v250, 0
	v_readlane_b32 s93, v250, 1
	v_readlane_b32 s94, v250, 2
	v_readlane_b32 s95, v250, 3
	v_lshlrev_b32_e32 v4, 2, v0
	v_and_b32_e32 v12, 12, v4
	v_bfe_u32 v13, v2, 2, 2
	v_lshl_add_u32 v14, v0, 8, s14
	v_bitop3_b32 v4, v12, v3, v13 bitop3:0x36
	v_readlane_b32 s4, v250, 13
	v_lshl_add_u32 v243, v4, 4, v14
	v_or_b32_e32 v15, s13, v0
	v_mul_u32_u24_e32 v8, 0x210, v15
	v_lshlrev_b32_e32 v9, 4, v3
	v_add3_u32 v242, 0, v8, v9
	v_lshlrev_b32_e32 v246, 3, v3
	v_mov_b32_e32 v247, s4
	s_movk_i32 s4, 0x90
	v_mad_u32_u24 v247, v15, s4, v247
	v_add3_u32 v149, v247, v246, s15
	ds_read_b128 v[4:7], v243 offset:33792
	ds_read_b128 v[8:11], v242
	v_xor_b32_e32 v245, 32, v243
	ds_read_b128 v[12:15], v245 offset:33792
	ds_read_b128 v[226:229], v242 offset:32
	v_xor_b32_e32 v244, 64, v243
	ds_read_b128 v[230:233], v244 offset:33792
	ds_read_b128 v[238:241], v242 offset:64
	s_waitcnt lgkmcnt(4)
	v_mfma_f32_32x32x16_bf16 v[80:95], v[4:7], v[8:11], 0
	v_xor_b32_e32 v245, 0x60, v243
	ds_read_b128 v[4:7], v245 offset:33792
	ds_read_b128 v[8:11], v242 offset:96
	s_waitcnt lgkmcnt(4)
	v_mfma_f32_32x32x16_bf16 v[80:95], v[12:15], v[226:229], v[80:95]
	s_add_i32 s101, s100, 0x180000
	buffer_load_dwordx4 v[96:99], v167, s[92:95], s101 offen
	v_xor_b32_e32 v244, 0x80, v243
	ds_read_b128 v[12:15], v244 offset:33792
	ds_read_b128 v[226:229], v242 offset:128
	s_waitcnt lgkmcnt(4)
	v_mfma_f32_32x32x16_bf16 v[80:95], v[230:233], v[238:241], v[80:95]
	s_add_i32 s101, s100, 0x181000
	buffer_load_dwordx4 v[100:103], v167, s[92:95], s101 offen
	v_xor_b32_e32 v245, 0xa0, v243
	ds_read_b128 v[230:233], v245 offset:33792
	ds_read_b128 v[238:241], v242 offset:160
	s_waitcnt lgkmcnt(4)
	v_mfma_f32_32x32x16_bf16 v[80:95], v[4:7], v[8:11], v[80:95]
	s_add_i32 s101, s100, 0x1e0000
	buffer_load_dwordx4 v[104:107], v167, s[92:95], s101 offen
	v_xor_b32_e32 v244, 0xc0, v243
	ds_read_b128 v[4:7], v244 offset:33792
	ds_read_b128 v[8:11], v242 offset:192
	s_waitcnt lgkmcnt(4)
	v_mfma_f32_32x32x16_bf16 v[80:95], v[12:15], v[226:229], v[80:95]
	s_add_i32 s101, s100, 0x1e1000
	buffer_load_dwordx4 v[108:111], v167, s[92:95], s101 offen
	v_xor_b32_e32 v245, 0xe0, v243
	ds_read_b128 v[12:15], v245 offset:33792
	ds_read_b128 v[226:229], v242 offset:224
	s_waitcnt lgkmcnt(4)
	v_mfma_f32_32x32x16_bf16 v[80:95], v[230:233], v[238:241], v[80:95]
	s_add_i32 s101, s100, 0x240000
	buffer_load_dwordx4 v[112:115], v167, s[92:95], s101 offen
	ds_read_b128 v[230:233], v243 offset:50176
	ds_read_b128 v[238:241], v242 offset:256
	s_waitcnt lgkmcnt(4)
	v_mfma_f32_32x32x16_bf16 v[80:95], v[4:7], v[8:11], v[80:95]
	s_add_i32 s101, s100, 0x241000
	buffer_load_dwordx4 v[116:119], v167, s[92:95], s101 offen
	v_xor_b32_e32 v245, 32, v243
	ds_read_b128 v[4:7], v245 offset:50176
	ds_read_b128 v[8:11], v242 offset:288
	s_waitcnt lgkmcnt(4)
	v_mfma_f32_32x32x16_bf16 v[80:95], v[12:15], v[226:229], v[80:95]
	s_add_i32 s101, s100, 0x2a0000
	buffer_load_dwordx4 v[120:123], v167, s[92:95], s101 offen
	v_xor_b32_e32 v244, 64, v243
	ds_read_b128 v[12:15], v244 offset:50176
	ds_read_b128 v[226:229], v242 offset:320
	s_waitcnt lgkmcnt(4)
	v_mfma_f32_32x32x16_bf16 v[80:95], v[230:233], v[238:241], v[80:95]
	s_add_i32 s101, s100, 0x2a1000
	buffer_load_dwordx4 v[124:127], v167, s[92:95], s101 offen
	v_xor_b32_e32 v245, 0x60, v243
	ds_read_b128 v[230:233], v245 offset:50176
	ds_read_b128 v[238:241], v242 offset:352
	s_waitcnt lgkmcnt(4)
	v_mfma_f32_32x32x16_bf16 v[80:95], v[4:7], v[8:11], v[80:95]
	s_add_i32 s101, s26, s80
	buffer_load_dwordx4 v[128:131], v168, s[92:95], s101 offen
	v_xor_b32_e32 v244, 0x80, v243
	ds_read_b128 v[4:7], v244 offset:50176
	ds_read_b128 v[8:11], v242 offset:384
	s_waitcnt lgkmcnt(4)
	v_mfma_f32_32x32x16_bf16 v[80:95], v[12:15], v[226:229], v[80:95]
	v_xor_b32_e32 v245, 0xa0, v243
	ds_read_b128 v[12:15], v245 offset:50176
	ds_read_b128 v[226:229], v242 offset:416
	s_waitcnt lgkmcnt(4)
	v_mfma_f32_32x32x16_bf16 v[80:95], v[230:233], v[238:241], v[80:95]
	v_xor_b32_e32 v244, 0xc0, v243
	ds_read_b128 v[230:233], v244 offset:50176
	ds_read_b128 v[238:241], v242 offset:448
	s_waitcnt lgkmcnt(4)
	v_mfma_f32_32x32x16_bf16 v[80:95], v[4:7], v[8:11], v[80:95]
	v_xor_b32_e32 v245, 0xe0, v243
	ds_read_b128 v[4:7], v245 offset:50176
	ds_read_b128 v[8:11], v242 offset:480
	s_waitcnt lgkmcnt(4)
	v_mfma_f32_32x32x16_bf16 v[80:95], v[12:15], v[226:229], v[80:95]
	s_waitcnt lgkmcnt(2)
	v_mfma_f32_32x32x16_bf16 v[80:95], v[230:233], v[238:241], v[80:95]
	s_waitcnt lgkmcnt(0)
	v_mfma_f32_32x32x16_bf16 v[80:95], v[4:7], v[8:11], v[80:95]
	s_nop 11
	v_pk_mul_f32 v[4:5], v[132:133], v[80:81]
	v_pk_mul_f32 v[6:7], v[134:135], v[82:83]
	v_pk_mul_f32 v[8:9], v[136:137], v[84:85]
	v_pk_mul_f32 v[10:11], v[138:139], v[86:87]
	v_pk_mul_f32 v[12:13], v[140:141], v[88:89]
	v_pk_mul_f32 v[14:15], v[142:143], v[90:91]
	v_pk_mul_f32 v[238:239], v[144:145], v[92:93]
	v_pk_mul_f32 v[240:241], v[146:147], v[94:95]
	v_cvt_pk_bf16_f32 v4, v4, v5
	v_cvt_pk_bf16_f32 v5, v6, v7
	v_cvt_pk_bf16_f32 v6, v8, v9
	v_cvt_pk_bf16_f32 v7, v10, v11
	v_cvt_pk_bf16_f32 v8, v12, v13
	v_cvt_pk_bf16_f32 v9, v14, v15
	v_cvt_pk_bf16_f32 v10, v238, v239
	v_cvt_pk_bf16_f32 v11, v240, v241
	ds_write2_b64 v149, v[4:5], v[6:7] offset1:2
	ds_write2_b64 v149, v[8:9], v[10:11] offset0:4 offset1:6

; #define LAS __attribute__((address_space(3)))
; __device__ __forceinline__ unsigned pk2(float lo, float hi) { const pk_f2 v = {lo, hi}; return __builtin_bit_cast(unsigned, __builtin_convertvector(v, pk_b2)); }
; #define RS_MMA4(fa, fb) do { _Pragma("unroll") for (int j = 0; j < 4; ++j) acc = mfma32(fa[j], fb[j], acc); } while (0)
; __device__ __forceinline__ void phase_ret_scan(const bf16* PROJ, bf16* O, LAS unsigned char* lds, int tid, int vcu, int G) {
;     ...
; #pragma unroll
;                 for (int ks = 0; ks < 4; ++ks) { fa0[ks] = *(const LAS s16x8*)(lds + PI + (32 * ti + a31) * PRS + (16 * ks + 8 * a5) * 2); fb0[ks] = tr_frag_b2(lds + VV, trb_base(lnA, vi, 0), trb_base(lnA, vi, 1), ks); }
;                 RS_MMA4(fa0, fb0);
; #pragma unroll
;                 for (int i = 0; i < 8; ++i) { const float o0_ = acc[2 * i], o1_ = acc[2 * i + 1]; opk[i] = pk2(o0_, o1_); }
;             }
;     ...
;             __syncthreads();
;         }
;         RS_STORE_O(SEQ / 64 - 1);
.Lrf_649:
	s_andn2_b64 vcc, exec, s[8:9]
	s_cbranch_vccz .Lrf_637
	v_readlane_b32 s92, v250, 4
	v_readlane_b32 s93, v250, 5
	v_readlane_b32 s94, v250, 6
	v_readlane_b32 s95, v250, 7
	ds_write_b16 v190, v4
	ds_write_b16_d16_hi v190, v4 offset:80
	ds_write_b16 v190, v5 offset:160
	ds_write_b16_d16_hi v190, v5 offset:240
	ds_write_b16 v190, v6 offset:640
	ds_write_b16_d16_hi v190, v6 offset:720
	ds_write_b16 v190, v7 offset:800
	ds_write_b16_d16_hi v190, v7 offset:880
	ds_write_b16 v190, v8 offset:1280
	ds_write_b16_d16_hi v190, v8 offset:1360
	ds_write_b16 v190, v9 offset:1440
	ds_write_b16_d16_hi v190, v9 offset:1520
	ds_write_b16 v190, v10 offset:1920
	ds_write_b16_d16_hi v190, v10 offset:2000
	ds_write_b16 v190, v11 offset:2080
	ds_write_b16_d16_hi v190, v11 offset:2160
	s_waitcnt lgkmcnt(0)
	ds_read_b128 v[16:19], v191
	ds_read_b128 v[20:23], v191 offset:1280
	s_add_i32 s101, s81, 0x20000
	s_waitcnt lgkmcnt(0)
	buffer_store_dwordx4 v[16:19], v201, s[92:95], s81 offen
	buffer_store_dwordx4 v[20:23], v201, s[92:95], s101 offen
	s_branch .Lrf_638
.Lrf_651:
	s_waitcnt vmcnt(0)
	s_branch .LBB0_568

; __global__ void __launch_bounds__(NWAVES * 64, 2) trunk_fwd(Args a) {
;     extern __shared__ __attribute__((aligned(16))) unsigned char lds_raw[];
	.amdhsa_kernel _Z9trunk_fwd4Args
		.amdhsa_group_segment_fixed_size 0
		.amdhsa_private_segment_fixed_size 0
		.amdhsa_kernarg_size 432
		.amdhsa_user_sgpr_count 2
		.amdhsa_user_sgpr_dispatch_ptr 0
		.amdhsa_user_sgpr_queue_ptr 0
		.amdhsa_user_sgpr_kernarg_segment_ptr 1
		.amdhsa_user_sgpr_dispatch_id 0
		.amdhsa_user_sgpr_kernarg_preload_length 0
		.amdhsa_user_sgpr_kernarg_preload_offset 0
		.amdhsa_user_sgpr_private_segment_size 0
		.amdhsa_uses_dynamic_stack 0
		.amdhsa_enable_private_segment 0
		.amdhsa_system_sgpr_workgroup_id_x 1
		.amdhsa_system_sgpr_workgroup_id_y 0
		.amdhsa_system_sgpr_workgroup_id_z 0
		.amdhsa_system_sgpr_workgroup_info 0
		.amdhsa_system_vgpr_workitem_id 0
		.amdhsa_next_free_vgpr 253
		.amdhsa_next_free_sgpr 102
		.amdhsa_accum_offset 256
		.amdhsa_reserve_vcc 1
		.amdhsa_float_round_mode_32 0
		.amdhsa_float_round_mode_16_64 0
		.amdhsa_float_denorm_mode_32 3
		.amdhsa_float_denorm_mode_16_64 3
		.amdhsa_dx10_clamp 1
		.amdhsa_ieee_mode 1
		.amdhsa_fp16_overflow 0
		.amdhsa_tg_split 0
		.amdhsa_exception_fp_ieee_invalid_op 0
		.amdhsa_exception_fp_denorm_src 0
		.amdhsa_exception_fp_ieee_div_zero 0
		.amdhsa_exception_fp_ieee_overflow 0
		.amdhsa_exception_fp_ieee_underflow 0
		.amdhsa_exception_fp_ieee_inexact 0
		.amdhsa_exception_int_div_zero 0
	.end_amdhsa_kernel

; __global__ void __launch_bounds__(NWAVES * 64, 2) trunk_fwd(Args a) {
;     extern __shared__ __attribute__((aligned(16))) unsigned char lds_raw[];
amdhsa.kernels:
  - .agpr_count:     0
    .args:
      - .offset:         0
        .size:           176
        .value_kind:     by_value
      - .offset:         176
        .size:           4
        .value_kind:     hidden_block_count_x
      - .offset:         180
        .size:           4
        .value_kind:     hidden_block_count_y
      - .offset:         184
        .size:           4
        .value_kind:     hidden_block_count_z
      - .offset:         188
        .size:           2
        .value_kind:     hidden_group_size_x
      - .offset:         190
        .size:           2
        .value_kind:     hidden_group_size_y
      - .offset:         192
        .size:           2
        .value_kind:     hidden_group_size_z
      - .offset:         194
        .size:           2
        .value_kind:     hidden_remainder_x
      - .offset:         196
        .size:           2
        .value_kind:     hidden_remainder_y
      - .offset:         198
        .size:           2
        .value_kind:     hidden_remainder_z
      - .offset:         216
        .size:           8
        .value_kind:     hidden_global_offset_x
      - .offset:         224
        .size:           8
        .value_kind:     hidden_global_offset_y
      - .offset:         232
        .size:           8
        .value_kind:     hidden_global_offset_z
      - .offset:         240
        .size:           2
        .value_kind:     hidden_grid_dims
      - .offset:         296
        .size:           4
        .value_kind:     hidden_dynamic_lds_size
    .group_segment_fixed_size: 0
    .kernarg_segment_align: 8
    .kernarg_segment_size: 432
    .language:       OpenCL C
    .language_version:
      - 2
      - 0
    .max_flat_workgroup_size: 512
    .name:           _Z9trunk_fwd4Args
    .private_segment_fixed_size: 0
    .sgpr_count:     108
    .sgpr_spill_count: 385
    .symbol:         _Z9trunk_fwd4Args.kd
    .uniform_work_group_size: 1
    .uses_dynamic_stack: false
    .vgpr_count:     253
    .vgpr_spill_count: 0
    .wavefront_size: 64
